# grid barrier between the compressed-attention and selected-attention phases removed: the selection masks and the o rows a workgroup reads there are the ones it wrote itself (same unit mapping), workgr
# speedup vs baseline: 1.0065x; 1.0065x over previous
; __device__ __forceinline__ unsigned xb_ld(unsigned* p)              { return __hip_atomic_load(p, __ATOMIC_RELAXED, __HIP_MEMORY_SCOPE_AGENT); }
; __device__ __forceinline__ unsigned xb_add(unsigned* p, unsigned v) { return __hip_atomic_fetch_add(p, v, __ATOMIC_RELAXED, __HIP_MEMORY_SCOPE_AGENT); }
; #define XB_SPIN(cond, bar) do { unsigned _sp = 0; while (cond) { __builtin_amdgcn_s_sleep(1); \
;     if ((++_sp & 255u) == 0u) { if (xb_ld(&(bar)[XB_TMO])) break; if (_sp > XB_SPIN_CAP) { atomicAdd(&(bar)[XB_TMO], 1u); break; } } } } while (0)
; #define DUPBAR() do { PHASE_BEGIN(); xcd_barrier(bar, F.tid); } while (0)
; #define SEAM(k) do { PHASE_BEGIN(); if (IN(k) && (k) + 1 < hi && (((MK_MASK) >> ((k) + 1)) != 0)) xcd_barrier(bar, F.tid); } while (0)
; __device__ __forceinline__ void xcd_barrier(const XcdBarrier& b, int tid) {
;     asm volatile("s_waitcnt vmcnt(0)" ::: "memory");
;     __syncthreads();
;     if (tid == 0) {
;         unsigned* bar = b.bar;
;         __builtin_amdgcn_s_waitcnt(0);
;         unsigned nloc = b.st[0], nx = b.st[1];
;         if (nloc == 0u) { xcd_barrier_complete(bar, b.x, nloc, nx); b.st[0] = nloc; b.st[1] = nx; }
;         const unsigned old = xb_add(&bar[XB_XSUB(b.x)], 1u);
;         const unsigned gen = old / nloc;
;         if (old + 1u == (gen + 1u) * nloc) {
;             __builtin_amdgcn_fence(__ATOMIC_RELEASE, "agent");
;             asm volatile("s_waitcnt vmcnt(0)" ::: "memory");
;             const unsigned og = xb_add(&bar[XB_TOP], 1u);
;             const unsigned tg = og / nx;
;             if (og + 1u == (tg + 1u) * nx) xb_add(&bar[XB_TOPGEN], 1u);
;             else XB_SPIN(xb_ld(&bar[XB_TOPGEN]) == tg, bar);
;             __builtin_amdgcn_fence(__ATOMIC_ACQUIRE, "agent");
;             xb_add(&bar[XB_XGEN(b.x)], 1u);
;             asm volatile("s_waitcnt vmcnt(0)" ::: "memory");
;         } else {
;             XB_SPIN(xb_ld(&bar[XB_XGEN(b.x)]) == gen, bar);
;             __builtin_amdgcn_fence(__ATOMIC_ACQUIRE, "agent");
;             asm volatile("s_waitcnt vmcnt(0)" ::: "memory");
;         }
;     }
;     __syncthreads();
; }
; __global__ void __launch_bounds__(NTHR, 2) mega_fwd(Args args) {
;     ...
;     if (IN(12)) { cmp_phase(F); if (DUP(12)) { DUPBAR(); cmp_phase(F); } } SEAM(12);
;     if (IN(13)) { if (DUP(13)) { sel_phase<true>(F); DUPBAR(); } sel_phase<false>(F); } SEAM(13);
.LBB0_1636:
	s_cmp_gt_i32 s93, 13
	s_cselect_b64 s[2:3], -1, 0
	s_and_b64 s[4:5], s[42:43], s[2:3]
	s_andn2_b64 vcc, exec, s[4:5]
	v_readlane_b32 s4, v238, 2
	s_waitcnt vmcnt(0)
	v_mbcnt_lo_u32_b32 v2, -1, 0
	v_mbcnt_hi_u32_b32 v2, -1, v2
	s_nop 0
	v_add_u32_e32 v100, s4, v2
	s_branch .LBB0_1690
